# full stack: P1/P4/P5/P6/P7/P11 load pipelining, P9 token loads + bias loads hoisted, barrier non-leaders poll cross-XCD generation
# baseline (speedup 1.0000x reference)
; template <class Epi, class Sched, bool ALIGN_EPI = false, bool SP2 = false, bool F8 = false, bool GATHER = false>
; __device__ __forceinline__ void gemm_phase(PG8_LAS unsigned char* lds, const Gemm g, const Sched& S, const Epi& E) {
;     ...
; #pragma unroll
;         for (int a = 0; a < 2; ++a)
; #pragma unroll
;             for (int b = 0; b < 2; ++b)
; #pragma unroll
;                 for (int m = 0; m < 4; ++m)
; #pragma unroll
;                     for (int n = 0; n < 2; ++n) acc[a][b][m][n] = (f32x4){0.f, 0.f, 0.f, 0.f};
;     __device__ __forceinline__ void operator()(const f32x4 (&acc)[2][2][4][2], const Unit& u, int wr, int wc, int fr, int fq) const {
;         const int e = u.pn >> 4, pnl = u.pn & 15; const int row0 = u.pm * BM + wr * 64 + fr; const int col0 = pnl * HALF + wc * 32 + 8 * fq;
;         f32x4 bgv[2], buv[2];
; #pragma unroll
;         for (int n = 0; n < 2; ++n) { bgv[n] = *(const f32x4*)(bg + (size_t)e * 2048 + col0 + 4 * n); buv[n] = *(const f32x4*)(bu + (size_t)e * 2048 + col0 + 4 * n); }
.LBB0_995:
	s_ashr_i32 s70, s46, 4
	s_lshl_b32 s72, s46, 7
	s_ashr_i32 s71, s70, 31
	s_and_b32 s72, s72, 0x780
	s_lshl_b64 s[70:71], s[70:71], 13
	v_or_b32_e32 v2, s72, v195
	v_lshlrev_b32_e32 v2, 2, v2
	s_add_u32 s72, s16, s70
	s_addc_u32 s73, s17, s71
	global_load_dwordx4 v[240:243], v2, s[72:73]
	global_load_dwordx4 v[248:251], v2, s[72:73] offset:16
	s_add_u32 s70, s20, s70
	s_addc_u32 s71, s21, s71
	global_load_dwordx4 v[252:255], v2, s[70:71]
	global_load_dwordx2 v[244:245], v2, s[70:71] offset:16
	global_load_dword v247, v2, s[70:71] offset:24
	global_load_dword v190, v2, s[70:71] offset:28
	s_ashr_i32 s43, s42, 31
	s_lshl_b64 s[44:45], s[42:43], 19
	s_add_u32 s44, s2, s44
	s_addc_u32 s45, s3, s45
	s_and_b64 s[50:51], s[50:51], exec
	s_cselect_b32 s43, s45, s49
	s_cselect_b32 s63, s44, s48
	v_mov_b32_e32 v169, v163
	v_mov_b32_e32 v173, v163
	s_add_u32 s64, s48, 0x100
	v_mov_b32_e32 v34, 0
	v_lshl_add_u64 v[174:175], s[36:37], 0, v[172:173]
	v_lshl_add_u64 v[176:177], s[36:37], 0, v[168:169]
	s_addc_u32 s65, s49, 0
	s_mov_b32 s66, -2
	s_mov_b64 s[48:49], 0
	v_mov_b32_e32 v35, v34
	v_mov_b32_e32 v36, v34
	v_mov_b32_e32 v37, v34
	v_mov_b32_e32 v42, v34
	v_mov_b32_e32 v43, v34
	v_mov_b32_e32 v44, v34
	v_mov_b32_e32 v45, v34
	v_mov_b32_e32 v50, v34
	v_mov_b32_e32 v51, v34
	v_mov_b32_e32 v52, v34
	v_mov_b32_e32 v53, v34
	v_mov_b32_e32 v58, v34
	v_mov_b32_e32 v59, v34
	v_mov_b32_e32 v60, v34
	v_mov_b32_e32 v61, v34
	v_mov_b32_e32 v66, v34
	v_mov_b32_e32 v67, v34
	v_mov_b32_e32 v68, v34
	v_mov_b32_e32 v69, v34
	v_mov_b32_e32 v74, v34
	v_mov_b32_e32 v75, v34
	v_mov_b32_e32 v76, v34
	v_mov_b32_e32 v77, v34
	v_mov_b32_e32 v82, v34
	v_mov_b32_e32 v83, v34
	v_mov_b32_e32 v84, v34
	v_mov_b32_e32 v85, v34
	v_mov_b32_e32 v90, v34
	v_mov_b32_e32 v91, v34
	v_mov_b32_e32 v92, v34
	v_mov_b32_e32 v93, v34
	v_mov_b32_e32 v38, v34
	v_mov_b32_e32 v39, v34
	v_mov_b32_e32 v40, v34
	v_mov_b32_e32 v41, v34
	v_mov_b32_e32 v46, v34
	v_mov_b32_e32 v47, v34
	v_mov_b32_e32 v48, v34
	v_mov_b32_e32 v49, v34
	v_mov_b32_e32 v54, v34
	v_mov_b32_e32 v55, v34
	v_mov_b32_e32 v56, v34
	v_mov_b32_e32 v57, v34
	v_mov_b32_e32 v62, v34
	v_mov_b32_e32 v63, v34
	v_mov_b32_e32 v64, v34
	v_mov_b32_e32 v65, v34
	v_mov_b32_e32 v70, v34
	v_mov_b32_e32 v71, v34
	v_mov_b32_e32 v72, v34
	v_mov_b32_e32 v73, v34
	v_mov_b32_e32 v78, v34
	v_mov_b32_e32 v79, v34
	v_mov_b32_e32 v80, v34
	v_mov_b32_e32 v81, v34
	v_mov_b32_e32 v86, v34
	v_mov_b32_e32 v87, v34
	v_mov_b32_e32 v88, v34
	v_mov_b32_e32 v89, v34
	v_mov_b32_e32 v94, v34
	v_mov_b32_e32 v95, v34
	v_mov_b32_e32 v96, v34
	v_mov_b32_e32 v97, v34
	v_mov_b32_e32 v98, v34
	v_mov_b32_e32 v99, v34
	v_mov_b32_e32 v100, v34
	v_mov_b32_e32 v101, v34
	v_mov_b32_e32 v106, v34
	v_mov_b32_e32 v107, v34
	v_mov_b32_e32 v108, v34
	v_mov_b32_e32 v109, v34
	v_mov_b32_e32 v114, v34
	v_mov_b32_e32 v115, v34
	v_mov_b32_e32 v116, v34
	v_mov_b32_e32 v117, v34
	v_mov_b32_e32 v122, v34
	v_mov_b32_e32 v123, v34
	v_mov_b32_e32 v124, v34
	v_mov_b32_e32 v125, v34
	v_mov_b32_e32 v130, v34
	v_mov_b32_e32 v131, v34
	v_mov_b32_e32 v132, v34
	v_mov_b32_e32 v133, v34
	v_mov_b32_e32 v138, v34
	v_mov_b32_e32 v139, v34
	v_mov_b32_e32 v140, v34
	v_mov_b32_e32 v141, v34
	v_mov_b32_e32 v146, v34
	v_mov_b32_e32 v147, v34
	v_mov_b32_e32 v148, v34
	v_mov_b32_e32 v149, v34
	v_mov_b32_e32 v150, v34
	v_mov_b32_e32 v151, v34
	v_mov_b32_e32 v152, v34
	v_mov_b32_e32 v153, v34
	v_mov_b32_e32 v102, v34
	v_mov_b32_e32 v103, v34
	v_mov_b32_e32 v104, v34
	v_mov_b32_e32 v105, v34
	v_mov_b32_e32 v110, v34
	v_mov_b32_e32 v111, v34
	v_mov_b32_e32 v112, v34
	v_mov_b32_e32 v113, v34
	v_mov_b32_e32 v118, v34
	v_mov_b32_e32 v119, v34
	v_mov_b32_e32 v120, v34
	v_mov_b32_e32 v121, v34
	v_mov_b32_e32 v126, v34
	v_mov_b32_e32 v127, v34
	v_mov_b32_e32 v128, v34
	v_mov_b32_e32 v129, v34
	v_mov_b32_e32 v134, v34
	v_mov_b32_e32 v135, v34
	v_mov_b32_e32 v136, v34
	v_mov_b32_e32 v137, v34
	v_mov_b32_e32 v142, v34
	v_mov_b32_e32 v143, v34
	v_mov_b32_e32 v144, v34
	v_mov_b32_e32 v145, v34
	v_mov_b32_e32 v154, v34
	v_mov_b32_e32 v155, v34
	v_mov_b32_e32 v156, v34
	v_mov_b32_e32 v157, v34
	v_mov_b32_e32 v158, v34
	v_mov_b32_e32 v159, v34
	v_mov_b32_e32 v160, v34
	v_mov_b32_e32 v161, v34

; #define PG8_WAIT_V(n) asm volatile("s_waitcnt vmcnt(" #n ")" ::: "memory")
; #define PG8_BAR __builtin_amdgcn_s_barrier()
; template <class Epi, class Sched, bool ALIGN_EPI = false, bool SP2 = false, bool F8 = false, bool GATHER = false>
; __device__ __forceinline__ void gemm_phase(PG8_LAS unsigned char* lds, const Gemm g, const Sched& S, const Epi& E) {
;     ...
;     PG8_WAIT_V(0);
;     if constexpr (!ALIGN_EPI) { if (wr == 0) PG8_BAR; }
;     PG8_BAR;
.LBB0_1002:
	s_mov_b64 s[70:71], exec
	s_mov_b64 exec, -1
	v_mbcnt_lo_u32_b32 v190, -1, 0
	s_mov_b64 exec, s[70:71]
	s_waitcnt vmcnt(0)
	s_barrier
